# router phase prologue: the 128 router-weight loads per lane issued as a rolling window of 48 in flight with in-place hi/lo bf16 split (was 16 serial groups of 8 with a full drain each)
# baseline (speedup 1.0000x reference)
; __device__ __forceinline__ unsigned cvt_pk_bf16(float lo, float hi) { unsigned r; asm volatile("v_cvt_pk_bf16_f32 %0, %1, %2" : "=v"(r) : "v"(lo), "v"(hi)); return r; }
; __device__ __forceinline__ void phase5(Frame& F, const Args& a) {
;     ...
;     bf16x8_t wh[8][2], wl[8][2];
;     { const float* wp = a.rw + (size_t)(wid * 256 + 8 * (lane >> 4)) * NE + (lane & 15);
; #pragma unroll
;         for (int sk = 0; sk < 8; ++sk)
; #pragma unroll
;             for (int nt = 0; nt < 2; ++nt) { float w8[8];
; #pragma unroll
;                 for (int t = 0; t < 8; ++t) w8[t] = wp[(size_t)(32 * sk + t) * NE + 16 * nt];
;                 pg8::u32x4 hv, lv;
; #pragma unroll
;                 for (int t2 = 0; t2 < 4; ++t2) { const unsigned h = pg8::cvt_pk_bf16(w8[2 * t2], w8[2 * t2 + 1]); hv[t2] = h; lv[t2] = pg8::cvt_pk_bf16(w8[2 * t2] - bflo(h), w8[2 * t2 + 1] - bfhi(h)); }
;                 wh[sk][nt] = __builtin_bit_cast(bf16x8_t, hv); wl[sk][nt] = __builtin_bit_cast(bf16x8_t, lv); } }
.LBB0_624:
	s_or_b64 exec, exec, s[0:1]
	s_add_u32 s12, s76, 0x20000000
	s_addc_u32 s13, s77, 0
	s_lshl_b32 s0, s49, 8
	v_bfe_u32 v131, v138, 4, 2
	v_readlane_b32 s52, v251, 2
	v_lshl_or_b32 v140, v131, 3, s0
	v_mov_b32_e32 v141, 0
	v_readlane_b32 s62, v251, 12
	v_readlane_b32 s63, v251, 13
	s_waitcnt vmcnt(19)
	v_lshlrev_b64 v[2:3], 7, v[140:141]
	s_mov_b64 s[14:15], s[62:63]
	v_and_b32_e32 v132, 15, v138
	v_lshl_add_u64 v[2:3], s[14:15], 0, v[2:3]
	v_lshlrev_b32_e32 v4, 2, v132
	v_mov_b32_e32 v5, v141
	s_waitcnt vmcnt(5)
	v_lshl_add_u64 v[106:107], v[2:3], 0, v[4:5]
	s_movk_i32 s0, 0x1000
	v_add_co_u32_e32 v26, vcc, s0, v106
	s_movk_i32 s1, 0x2000
	s_nop 1
	v_addc_co_u32_e32 v27, vcc, 0, v107, vcc
	v_add_co_u32_e32 v42, vcc, s1, v106
	s_movk_i32 s0, 0x3000
	s_nop 1
	v_addc_co_u32_e32 v43, vcc, 0, v107, vcc
	v_add_co_u32_e32 v58, vcc, s0, v106
	s_movk_i32 s1, 0x4000
	s_nop 1
	v_addc_co_u32_e32 v59, vcc, 0, v107, vcc
	v_add_co_u32_e32 v74, vcc, s1, v106
	s_movk_i32 s0, 0x5000
	s_nop 1
	v_addc_co_u32_e32 v75, vcc, 0, v107, vcc
	v_add_co_u32_e32 v90, vcc, s0, v106
	s_movk_i32 s1, 0x6000
	s_nop 1
	v_addc_co_u32_e32 v91, vcc, 0, v107, vcc
	v_add_co_u32_e32 v108, vcc, s1, v106
	s_movk_i32 s0, 0x7000
	s_nop 1
	v_addc_co_u32_e32 v109, vcc, 0, v107, vcc
	s_waitcnt vmcnt(1)
	v_add_co_u32_e32 v122, vcc, s0, v106
	s_add_i32 s0, s18, s49
	s_nop 1
	v_addc_co_u32_e32 v123, vcc, 0, v107, vcc
	s_ashr_i32 s1, s0, 31
	s_lshl_b64 s[4:5], s[0:1], 12
	v_readlane_b32 s64, v251, 14
	v_readlane_b32 s65, v251, 15
	v_and_b32_e32 v133, 63, v138
	s_add_u32 s4, s12, s4
	v_lshlrev_b32_e32 v130, 3, v133
	s_addc_u32 s5, s13, s5
	s_mov_b32 s1, 8
	s_mov_b32 s31, 0xffff0000
	s_mov_b32 s10, 0
	s_cmp_gt_i32 s30, 0
	v_readlane_b32 s53, v251, 3
	v_readlane_b32 s54, v251, 4
	v_readlane_b32 s55, v251, 5
	v_readlane_b32 s56, v251, 6
	v_readlane_b32 s57, v251, 7
	v_readlane_b32 s58, v251, 8
	v_readlane_b32 s59, v251, 9
	v_readlane_b32 s60, v251, 10
	v_readlane_b32 s61, v251, 11
	v_readlane_b32 s66, v251, 16
	v_readlane_b32 s67, v251, 17
	v_and_b32_e32 v1, 31, v138
	v_lshlrev_b32_e32 v137, 2, v1
	v_mov_b32_e32 v244, v106
	v_mov_b32_e32 v245, v107
	v_mov_b32_e32 v252, 0x1000
	v_mov_b32_e32 v253, 0
	global_load_dword v2, v[244:245], off
	global_load_dword v3, v[244:245], off offset:128
	global_load_dword v4, v[244:245], off offset:256
	global_load_dword v5, v[244:245], off offset:384
	global_load_dword v6, v[244:245], off offset:512
	global_load_dword v7, v[244:245], off offset:640
	global_load_dword v8, v[244:245], off offset:768
	global_load_dword v9, v[244:245], off offset:896
	global_load_dword v10, v[244:245], off offset:64
	global_load_dword v11, v[244:245], off offset:192
	global_load_dword v12, v[244:245], off offset:320
	global_load_dword v13, v[244:245], off offset:448
	global_load_dword v14, v[244:245], off offset:576
	global_load_dword v15, v[244:245], off offset:704
	global_load_dword v16, v[244:245], off offset:832
	global_load_dword v17, v[244:245], off offset:960
	v_lshl_add_u64 v[244:245], v[244:245], 0, v[252:253]
	global_load_dword v18, v[244:245], off
	global_load_dword v19, v[244:245], off offset:128
	global_load_dword v20, v[244:245], off offset:256
	global_load_dword v21, v[244:245], off offset:384
	global_load_dword v22, v[244:245], off offset:512
	global_load_dword v23, v[244:245], off offset:640
	global_load_dword v24, v[244:245], off offset:768
	global_load_dword v25, v[244:245], off offset:896
	global_load_dword v26, v[244:245], off offset:64
	global_load_dword v27, v[244:245], off offset:192
	global_load_dword v28, v[244:245], off offset:320
	global_load_dword v29, v[244:245], off offset:448
	global_load_dword v30, v[244:245], off offset:576
	global_load_dword v31, v[244:245], off offset:704
	global_load_dword v32, v[244:245], off offset:832
	global_load_dword v33, v[244:245], off offset:960
	v_lshl_add_u64 v[244:245], v[244:245], 0, v[252:253]
	global_load_dword v34, v[244:245], off
	global_load_dword v35, v[244:245], off offset:128
	global_load_dword v36, v[244:245], off offset:256
	global_load_dword v37, v[244:245], off offset:384
	global_load_dword v38, v[244:245], off offset:512
	global_load_dword v39, v[244:245], off offset:640
	global_load_dword v40, v[244:245], off offset:768
	global_load_dword v41, v[244:245], off offset:896
	global_load_dword v42, v[244:245], off offset:64
	global_load_dword v43, v[244:245], off offset:192
	global_load_dword v44, v[244:245], off offset:320
	global_load_dword v45, v[244:245], off offset:448
	global_load_dword v46, v[244:245], off offset:576
	global_load_dword v47, v[244:245], off offset:704
	global_load_dword v48, v[244:245], off offset:832
	global_load_dword v49, v[244:245], off offset:960
	v_lshl_add_u64 v[244:245], v[244:245], 0, v[252:253]
	s_waitcnt vmcnt(40)
	v_cvt_pk_bf16_f32 v243, v2, v3
	s_nop 0
	v_lshlrev_b32_e32 v249, 16, v243
	v_and_b32_e32 v250, 0xffff0000, v243
	v_sub_f32_e32 v249, v2, v249
	v_sub_f32_e32 v250, v3, v250
	v_cvt_pk_bf16_f32 v246, v249, v250
	v_cvt_pk_bf16_f32 v3, v4, v5
	s_nop 0
	v_lshlrev_b32_e32 v249, 16, v3
	v_and_b32_e32 v250, 0xffff0000, v3
	v_sub_f32_e32 v249, v4, v249
	v_sub_f32_e32 v250, v5, v250
	v_cvt_pk_bf16_f32 v247, v249, v250
	v_cvt_pk_bf16_f32 v4, v6, v7
	s_nop 0
	v_lshlrev_b32_e32 v249, 16, v4
	v_and_b32_e32 v250, 0xffff0000, v4
	v_sub_f32_e32 v249, v6, v249
	v_sub_f32_e32 v250, v7, v250
	v_cvt_pk_bf16_f32 v248, v249, v250
	v_cvt_pk_bf16_f32 v5, v8, v9
	s_nop 0
	v_lshlrev_b32_e32 v249, 16, v5
	v_and_b32_e32 v250, 0xffff0000, v5
	v_sub_f32_e32 v249, v8, v249
	v_sub_f32_e32 v250, v9, v250
	v_cvt_pk_bf16_f32 v9, v249, v250
	v_mov_b32_e32 v2, v243
	v_mov_b32_e32 v6, v246
	v_mov_b32_e32 v7, v247
	v_mov_b32_e32 v8, v248
	global_load_dword v50, v[244:245], off
	global_load_dword v51, v[244:245], off offset:128
	global_load_dword v52, v[244:245], off offset:256
	global_load_dword v53, v[244:245], off offset:384
	global_load_dword v54, v[244:245], off offset:512
	global_load_dword v55, v[244:245], off offset:640
	global_load_dword v56, v[244:245], off offset:768
	global_load_dword v57, v[244:245], off offset:896
	s_waitcnt vmcnt(40)
; __device__ __forceinline__ unsigned cvt_pk_bf16(float lo, float hi) { unsigned r; asm volatile("v_cvt_pk_bf16_f32 %0, %1, %2" : "=v"(r) : "v"(lo), "v"(hi)); return r; }
; __device__ __forceinline__ void phase5(Frame& F, const Args& a) {
;     ...
;     bf16x8_t wh[8][2], wl[8][2];
;     { const float* wp = a.rw + (size_t)(wid * 256 + 8 * (lane >> 4)) * NE + (lane & 15);
; #pragma unroll
;         for (int sk = 0; sk < 8; ++sk)
; #pragma unroll
;             for (int nt = 0; nt < 2; ++nt) { float w8[8];
; #pragma unroll
;                 for (int t = 0; t < 8; ++t) w8[t] = wp[(size_t)(32 * sk + t) * NE + 16 * nt];
;                 pg8::u32x4 hv, lv;
; #pragma unroll
;                 for (int t2 = 0; t2 < 4; ++t2) { const unsigned h = pg8::cvt_pk_bf16(w8[2 * t2], w8[2 * t2 + 1]); hv[t2] = h; lv[t2] = pg8::cvt_pk_bf16(w8[2 * t2] - bflo(h), w8[2 * t2 + 1] - bfhi(h)); }
;                 wh[sk][nt] = __builtin_bit_cast(bf16x8_t, hv); wl[sk][nt] = __builtin_bit_cast(bf16x8_t, lv); } }
	v_cvt_pk_bf16_f32 v243, v10, v11
	s_nop 0
	v_lshlrev_b32_e32 v249, 16, v243
	v_and_b32_e32 v250, 0xffff0000, v243
	v_sub_f32_e32 v249, v10, v249
	v_sub_f32_e32 v250, v11, v250
	v_cvt_pk_bf16_f32 v246, v249, v250
	v_cvt_pk_bf16_f32 v11, v12, v13
	s_nop 0
	v_lshlrev_b32_e32 v249, 16, v11
	v_and_b32_e32 v250, 0xffff0000, v11
	v_sub_f32_e32 v249, v12, v249
	v_sub_f32_e32 v250, v13, v250
	v_cvt_pk_bf16_f32 v247, v249, v250
	v_cvt_pk_bf16_f32 v12, v14, v15
	s_nop 0
	v_lshlrev_b32_e32 v249, 16, v12
	v_and_b32_e32 v250, 0xffff0000, v12
	v_sub_f32_e32 v249, v14, v249
	v_sub_f32_e32 v250, v15, v250
	v_cvt_pk_bf16_f32 v248, v249, v250
	v_cvt_pk_bf16_f32 v13, v16, v17
	s_nop 0
	v_lshlrev_b32_e32 v249, 16, v13
	v_and_b32_e32 v250, 0xffff0000, v13
	v_sub_f32_e32 v249, v16, v249
	v_sub_f32_e32 v250, v17, v250
	v_cvt_pk_bf16_f32 v17, v249, v250
	v_mov_b32_e32 v10, v243
	v_mov_b32_e32 v14, v246
	v_mov_b32_e32 v15, v247
	v_mov_b32_e32 v16, v248
	global_load_dword v58, v[244:245], off offset:64
	global_load_dword v59, v[244:245], off offset:192
	global_load_dword v60, v[244:245], off offset:320
	global_load_dword v61, v[244:245], off offset:448
	global_load_dword v62, v[244:245], off offset:576
	global_load_dword v63, v[244:245], off offset:704
	global_load_dword v64, v[244:245], off offset:832
	global_load_dword v65, v[244:245], off offset:960
	v_lshl_add_u64 v[244:245], v[244:245], 0, v[252:253]
	s_waitcnt vmcnt(40)
	v_cvt_pk_bf16_f32 v243, v18, v19
	s_nop 0
	v_lshlrev_b32_e32 v249, 16, v243
	v_and_b32_e32 v250, 0xffff0000, v243
	v_sub_f32_e32 v249, v18, v249
	v_sub_f32_e32 v250, v19, v250
	v_cvt_pk_bf16_f32 v246, v249, v250
	v_cvt_pk_bf16_f32 v19, v20, v21
	s_nop 0
	v_lshlrev_b32_e32 v249, 16, v19
	v_and_b32_e32 v250, 0xffff0000, v19
	v_sub_f32_e32 v249, v20, v249
	v_sub_f32_e32 v250, v21, v250
	v_cvt_pk_bf16_f32 v247, v249, v250
	v_cvt_pk_bf16_f32 v20, v22, v23
	s_nop 0
	v_lshlrev_b32_e32 v249, 16, v20
	v_and_b32_e32 v250, 0xffff0000, v20
	v_sub_f32_e32 v249, v22, v249
	v_sub_f32_e32 v250, v23, v250
	v_cvt_pk_bf16_f32 v248, v249, v250
	v_cvt_pk_bf16_f32 v21, v24, v25
	s_nop 0
	v_lshlrev_b32_e32 v249, 16, v21
	v_and_b32_e32 v250, 0xffff0000, v21
	v_sub_f32_e32 v249, v24, v249
	v_sub_f32_e32 v250, v25, v250
	v_cvt_pk_bf16_f32 v25, v249, v250
	v_mov_b32_e32 v18, v243
	v_mov_b32_e32 v22, v246
	v_mov_b32_e32 v23, v247
	v_mov_b32_e32 v24, v248
	global_load_dword v66, v[244:245], off
	global_load_dword v67, v[244:245], off offset:128
	global_load_dword v68, v[244:245], off offset:256
	global_load_dword v69, v[244:245], off offset:384
	global_load_dword v70, v[244:245], off offset:512
	global_load_dword v71, v[244:245], off offset:640
	global_load_dword v72, v[244:245], off offset:768
	global_load_dword v73, v[244:245], off offset:896
	s_waitcnt vmcnt(40)
	v_cvt_pk_bf16_f32 v243, v26, v27
	s_nop 0
	v_lshlrev_b32_e32 v249, 16, v243
	v_and_b32_e32 v250, 0xffff0000, v243
	v_sub_f32_e32 v249, v26, v249
	v_sub_f32_e32 v250, v27, v250
	v_cvt_pk_bf16_f32 v246, v249, v250
	v_cvt_pk_bf16_f32 v27, v28, v29
	s_nop 0
	v_lshlrev_b32_e32 v249, 16, v27
	v_and_b32_e32 v250, 0xffff0000, v27
	v_sub_f32_e32 v249, v28, v249
	v_sub_f32_e32 v250, v29, v250
	v_cvt_pk_bf16_f32 v247, v249, v250
	v_cvt_pk_bf16_f32 v28, v30, v31
	s_nop 0
	v_lshlrev_b32_e32 v249, 16, v28
	v_and_b32_e32 v250, 0xffff0000, v28
	v_sub_f32_e32 v249, v30, v249
	v_sub_f32_e32 v250, v31, v250
	v_cvt_pk_bf16_f32 v248, v249, v250
	v_cvt_pk_bf16_f32 v29, v32, v33
	s_nop 0
	v_lshlrev_b32_e32 v249, 16, v29
	v_and_b32_e32 v250, 0xffff0000, v29
	v_sub_f32_e32 v249, v32, v249
	v_sub_f32_e32 v250, v33, v250
	v_cvt_pk_bf16_f32 v33, v249, v250
	v_mov_b32_e32 v26, v243
	v_mov_b32_e32 v30, v246
	v_mov_b32_e32 v31, v247
	v_mov_b32_e32 v32, v248
	global_load_dword v74, v[244:245], off offset:64
	global_load_dword v75, v[244:245], off offset:192
	global_load_dword v76, v[244:245], off offset:320
	global_load_dword v77, v[244:245], off offset:448
	global_load_dword v78, v[244:245], off offset:576
	global_load_dword v79, v[244:245], off offset:704
	global_load_dword v80, v[244:245], off offset:832
	global_load_dword v81, v[244:245], off offset:960
	v_lshl_add_u64 v[244:245], v[244:245], 0, v[252:253]
	s_waitcnt vmcnt(40)
	v_cvt_pk_bf16_f32 v243, v34, v35
	s_nop 0
	v_lshlrev_b32_e32 v249, 16, v243
	v_and_b32_e32 v250, 0xffff0000, v243
	v_sub_f32_e32 v249, v34, v249
	v_sub_f32_e32 v250, v35, v250
	v_cvt_pk_bf16_f32 v246, v249, v250
	v_cvt_pk_bf16_f32 v35, v36, v37
	s_nop 0
	v_lshlrev_b32_e32 v249, 16, v35
	v_and_b32_e32 v250, 0xffff0000, v35
	v_sub_f32_e32 v249, v36, v249
	v_sub_f32_e32 v250, v37, v250
	v_cvt_pk_bf16_f32 v247, v249, v250
	v_cvt_pk_bf16_f32 v36, v38, v39
	s_nop 0
	v_lshlrev_b32_e32 v249, 16, v36
	v_and_b32_e32 v250, 0xffff0000, v36
	v_sub_f32_e32 v249, v38, v249
	v_sub_f32_e32 v250, v39, v250
	v_cvt_pk_bf16_f32 v248, v249, v250
	v_cvt_pk_bf16_f32 v37, v40, v41
	s_nop 0
	v_lshlrev_b32_e32 v249, 16, v37
	v_and_b32_e32 v250, 0xffff0000, v37
	v_sub_f32_e32 v249, v40, v249
	v_sub_f32_e32 v250, v41, v250
	v_cvt_pk_bf16_f32 v41, v249, v250
	v_mov_b32_e32 v34, v243
	v_mov_b32_e32 v38, v246
	v_mov_b32_e32 v39, v247
	v_mov_b32_e32 v40, v248
	global_load_dword v82, v[244:245], off
	global_load_dword v83, v[244:245], off offset:128
	global_load_dword v84, v[244:245], off offset:256
	global_load_dword v85, v[244:245], off offset:384
	global_load_dword v86, v[244:245], off offset:512
	global_load_dword v87, v[244:245], off offset:640
	global_load_dword v88, v[244:245], off offset:768
	global_load_dword v89, v[244:245], off offset:896
	s_waitcnt vmcnt(40)
; __device__ __forceinline__ unsigned cvt_pk_bf16(float lo, float hi) { unsigned r; asm volatile("v_cvt_pk_bf16_f32 %0, %1, %2" : "=v"(r) : "v"(lo), "v"(hi)); return r; }
; __device__ __forceinline__ void phase5(Frame& F, const Args& a) {
;     ...
;     bf16x8_t wh[8][2], wl[8][2];
;     { const float* wp = a.rw + (size_t)(wid * 256 + 8 * (lane >> 4)) * NE + (lane & 15);
; #pragma unroll
;         for (int sk = 0; sk < 8; ++sk)
; #pragma unroll
;             for (int nt = 0; nt < 2; ++nt) { float w8[8];
; #pragma unroll
;                 for (int t = 0; t < 8; ++t) w8[t] = wp[(size_t)(32 * sk + t) * NE + 16 * nt];
;                 pg8::u32x4 hv, lv;
; #pragma unroll
;                 for (int t2 = 0; t2 < 4; ++t2) { const unsigned h = pg8::cvt_pk_bf16(w8[2 * t2], w8[2 * t2 + 1]); hv[t2] = h; lv[t2] = pg8::cvt_pk_bf16(w8[2 * t2] - bflo(h), w8[2 * t2 + 1] - bfhi(h)); }
;                 wh[sk][nt] = __builtin_bit_cast(bf16x8_t, hv); wl[sk][nt] = __builtin_bit_cast(bf16x8_t, lv); } }
	v_cvt_pk_bf16_f32 v243, v42, v43
	s_nop 0
	v_lshlrev_b32_e32 v249, 16, v243
	v_and_b32_e32 v250, 0xffff0000, v243
	v_sub_f32_e32 v249, v42, v249
	v_sub_f32_e32 v250, v43, v250
	v_cvt_pk_bf16_f32 v246, v249, v250
	v_cvt_pk_bf16_f32 v43, v44, v45
	s_nop 0
	v_lshlrev_b32_e32 v249, 16, v43
	v_and_b32_e32 v250, 0xffff0000, v43
	v_sub_f32_e32 v249, v44, v249
	v_sub_f32_e32 v250, v45, v250
	v_cvt_pk_bf16_f32 v247, v249, v250
	v_cvt_pk_bf16_f32 v44, v46, v47
	s_nop 0
	v_lshlrev_b32_e32 v249, 16, v44
	v_and_b32_e32 v250, 0xffff0000, v44
	v_sub_f32_e32 v249, v46, v249
	v_sub_f32_e32 v250, v47, v250
	v_cvt_pk_bf16_f32 v248, v249, v250
	v_cvt_pk_bf16_f32 v45, v48, v49
	s_nop 0
	v_lshlrev_b32_e32 v249, 16, v45
	v_and_b32_e32 v250, 0xffff0000, v45
	v_sub_f32_e32 v249, v48, v249
	v_sub_f32_e32 v250, v49, v250
	v_cvt_pk_bf16_f32 v49, v249, v250
	v_mov_b32_e32 v42, v243
	v_mov_b32_e32 v46, v246
	v_mov_b32_e32 v47, v247
	v_mov_b32_e32 v48, v248
	global_load_dword v90, v[244:245], off offset:64
	global_load_dword v91, v[244:245], off offset:192
	global_load_dword v92, v[244:245], off offset:320
	global_load_dword v93, v[244:245], off offset:448
	global_load_dword v94, v[244:245], off offset:576
	global_load_dword v95, v[244:245], off offset:704
	global_load_dword v96, v[244:245], off offset:832
	global_load_dword v97, v[244:245], off offset:960
	v_lshl_add_u64 v[244:245], v[244:245], 0, v[252:253]
	s_waitcnt vmcnt(40)
	v_cvt_pk_bf16_f32 v243, v50, v51
	s_nop 0
	v_lshlrev_b32_e32 v249, 16, v243
	v_and_b32_e32 v250, 0xffff0000, v243
	v_sub_f32_e32 v249, v50, v249
	v_sub_f32_e32 v250, v51, v250
	v_cvt_pk_bf16_f32 v246, v249, v250
	v_cvt_pk_bf16_f32 v51, v52, v53
	s_nop 0
	v_lshlrev_b32_e32 v249, 16, v51
	v_and_b32_e32 v250, 0xffff0000, v51
	v_sub_f32_e32 v249, v52, v249
	v_sub_f32_e32 v250, v53, v250
	v_cvt_pk_bf16_f32 v247, v249, v250
	v_cvt_pk_bf16_f32 v52, v54, v55
	s_nop 0
	v_lshlrev_b32_e32 v249, 16, v52
	v_and_b32_e32 v250, 0xffff0000, v52
	v_sub_f32_e32 v249, v54, v249
	v_sub_f32_e32 v250, v55, v250
	v_cvt_pk_bf16_f32 v248, v249, v250
	v_cvt_pk_bf16_f32 v53, v56, v57
	s_nop 0
	v_lshlrev_b32_e32 v249, 16, v53
	v_and_b32_e32 v250, 0xffff0000, v53
	v_sub_f32_e32 v249, v56, v249
	v_sub_f32_e32 v250, v57, v250
	v_cvt_pk_bf16_f32 v57, v249, v250
	v_mov_b32_e32 v50, v243
	v_mov_b32_e32 v54, v246
	v_mov_b32_e32 v55, v247
	v_mov_b32_e32 v56, v248
	global_load_dword v98, v[244:245], off
	global_load_dword v99, v[244:245], off offset:128
	global_load_dword v100, v[244:245], off offset:256
	global_load_dword v101, v[244:245], off offset:384
	global_load_dword v102, v[244:245], off offset:512
	global_load_dword v103, v[244:245], off offset:640
	global_load_dword v104, v[244:245], off offset:768
	global_load_dword v105, v[244:245], off offset:896
	s_waitcnt vmcnt(40)
	v_cvt_pk_bf16_f32 v243, v58, v59
	s_nop 0
	v_lshlrev_b32_e32 v249, 16, v243
	v_and_b32_e32 v250, 0xffff0000, v243
	v_sub_f32_e32 v249, v58, v249
	v_sub_f32_e32 v250, v59, v250
	v_cvt_pk_bf16_f32 v246, v249, v250
	v_cvt_pk_bf16_f32 v59, v60, v61
	s_nop 0
	v_lshlrev_b32_e32 v249, 16, v59
	v_and_b32_e32 v250, 0xffff0000, v59
	v_sub_f32_e32 v249, v60, v249
	v_sub_f32_e32 v250, v61, v250
	v_cvt_pk_bf16_f32 v247, v249, v250
	v_cvt_pk_bf16_f32 v60, v62, v63
	s_nop 0
	v_lshlrev_b32_e32 v249, 16, v60
	v_and_b32_e32 v250, 0xffff0000, v60
	v_sub_f32_e32 v249, v62, v249
	v_sub_f32_e32 v250, v63, v250
	v_cvt_pk_bf16_f32 v248, v249, v250
	v_cvt_pk_bf16_f32 v61, v64, v65
	s_nop 0
	v_lshlrev_b32_e32 v249, 16, v61
	v_and_b32_e32 v250, 0xffff0000, v61
	v_sub_f32_e32 v249, v64, v249
	v_sub_f32_e32 v250, v65, v250
	v_cvt_pk_bf16_f32 v65, v249, v250
	v_mov_b32_e32 v58, v243
	v_mov_b32_e32 v62, v246
	v_mov_b32_e32 v63, v247
	v_mov_b32_e32 v64, v248
	global_load_dword v106, v[244:245], off offset:64
	global_load_dword v107, v[244:245], off offset:192
	global_load_dword v108, v[244:245], off offset:320
	global_load_dword v109, v[244:245], off offset:448
	global_load_dword v110, v[244:245], off offset:576
	global_load_dword v111, v[244:245], off offset:704
	global_load_dword v112, v[244:245], off offset:832
	global_load_dword v113, v[244:245], off offset:960
	v_lshl_add_u64 v[244:245], v[244:245], 0, v[252:253]
	s_waitcnt vmcnt(40)
	v_cvt_pk_bf16_f32 v243, v66, v67
	s_nop 0
	v_lshlrev_b32_e32 v249, 16, v243
	v_and_b32_e32 v250, 0xffff0000, v243
	v_sub_f32_e32 v249, v66, v249
	v_sub_f32_e32 v250, v67, v250
	v_cvt_pk_bf16_f32 v246, v249, v250
	v_cvt_pk_bf16_f32 v67, v68, v69
	s_nop 0
	v_lshlrev_b32_e32 v249, 16, v67
	v_and_b32_e32 v250, 0xffff0000, v67
	v_sub_f32_e32 v249, v68, v249
	v_sub_f32_e32 v250, v69, v250
	v_cvt_pk_bf16_f32 v247, v249, v250
	v_cvt_pk_bf16_f32 v68, v70, v71
	s_nop 0
	v_lshlrev_b32_e32 v249, 16, v68
	v_and_b32_e32 v250, 0xffff0000, v68
	v_sub_f32_e32 v249, v70, v249
	v_sub_f32_e32 v250, v71, v250
	v_cvt_pk_bf16_f32 v248, v249, v250
	v_cvt_pk_bf16_f32 v69, v72, v73
	s_nop 0
	v_lshlrev_b32_e32 v249, 16, v69
	v_and_b32_e32 v250, 0xffff0000, v69
	v_sub_f32_e32 v249, v72, v249
	v_sub_f32_e32 v250, v73, v250
	v_cvt_pk_bf16_f32 v73, v249, v250
	v_mov_b32_e32 v66, v243
	v_mov_b32_e32 v70, v246
	v_mov_b32_e32 v71, v247
	v_mov_b32_e32 v72, v248
	global_load_dword v114, v[244:245], off
	global_load_dword v115, v[244:245], off offset:128
	global_load_dword v116, v[244:245], off offset:256
	global_load_dword v117, v[244:245], off offset:384
	global_load_dword v118, v[244:245], off offset:512
	global_load_dword v119, v[244:245], off offset:640
	global_load_dword v120, v[244:245], off offset:768
	global_load_dword v121, v[244:245], off offset:896
	s_waitcnt vmcnt(40)
; __device__ __forceinline__ unsigned cvt_pk_bf16(float lo, float hi) { unsigned r; asm volatile("v_cvt_pk_bf16_f32 %0, %1, %2" : "=v"(r) : "v"(lo), "v"(hi)); return r; }
; __device__ __forceinline__ void phase5(Frame& F, const Args& a) {
;     ...
;     { const float* wp = a.rw + (size_t)(wid * 256 + 8 * (lane >> 4)) * NE + (lane & 15);
; #pragma unroll
;         for (int sk = 0; sk < 8; ++sk)
; #pragma unroll
;             for (int nt = 0; nt < 2; ++nt) { float w8[8];
; #pragma unroll
;                 for (int t = 0; t < 8; ++t) w8[t] = wp[(size_t)(32 * sk + t) * NE + 16 * nt];
;                 pg8::u32x4 hv, lv;
; #pragma unroll
;                 for (int t2 = 0; t2 < 4; ++t2) { const unsigned h = pg8::cvt_pk_bf16(w8[2 * t2], w8[2 * t2 + 1]); hv[t2] = h; lv[t2] = pg8::cvt_pk_bf16(w8[2 * t2] - bflo(h), w8[2 * t2 + 1] - bfhi(h)); }
;                 wh[sk][nt] = __builtin_bit_cast(bf16x8_t, hv); wl[sk][nt] = __builtin_bit_cast(bf16x8_t, lv); } }
	v_cvt_pk_bf16_f32 v243, v74, v75
	s_nop 0
	v_lshlrev_b32_e32 v249, 16, v243
	v_and_b32_e32 v250, 0xffff0000, v243
	v_sub_f32_e32 v249, v74, v249
	v_sub_f32_e32 v250, v75, v250
	v_cvt_pk_bf16_f32 v246, v249, v250
	v_cvt_pk_bf16_f32 v75, v76, v77
	s_nop 0
	v_lshlrev_b32_e32 v249, 16, v75
	v_and_b32_e32 v250, 0xffff0000, v75
	v_sub_f32_e32 v249, v76, v249
	v_sub_f32_e32 v250, v77, v250
	v_cvt_pk_bf16_f32 v247, v249, v250
	v_cvt_pk_bf16_f32 v76, v78, v79
	s_nop 0
	v_lshlrev_b32_e32 v249, 16, v76
	v_and_b32_e32 v250, 0xffff0000, v76
	v_sub_f32_e32 v249, v78, v249
	v_sub_f32_e32 v250, v79, v250
	v_cvt_pk_bf16_f32 v248, v249, v250
	v_cvt_pk_bf16_f32 v77, v80, v81
	s_nop 0
	v_lshlrev_b32_e32 v249, 16, v77
	v_and_b32_e32 v250, 0xffff0000, v77
	v_sub_f32_e32 v249, v80, v249
	v_sub_f32_e32 v250, v81, v250
	v_cvt_pk_bf16_f32 v81, v249, v250
	v_mov_b32_e32 v74, v243
	v_mov_b32_e32 v78, v246
	v_mov_b32_e32 v79, v247
	v_mov_b32_e32 v80, v248
	global_load_dword v122, v[244:245], off offset:64
	global_load_dword v123, v[244:245], off offset:192
	global_load_dword v124, v[244:245], off offset:320
	global_load_dword v125, v[244:245], off offset:448
	global_load_dword v126, v[244:245], off offset:576
	global_load_dword v127, v[244:245], off offset:704
	global_load_dword v128, v[244:245], off offset:832
	global_load_dword v129, v[244:245], off offset:960
	s_waitcnt vmcnt(40)
	v_cvt_pk_bf16_f32 v243, v82, v83
	s_nop 0
	v_lshlrev_b32_e32 v249, 16, v243
	v_and_b32_e32 v250, 0xffff0000, v243
	v_sub_f32_e32 v249, v82, v249
	v_sub_f32_e32 v250, v83, v250
	v_cvt_pk_bf16_f32 v246, v249, v250
	v_cvt_pk_bf16_f32 v83, v84, v85
	s_nop 0
	v_lshlrev_b32_e32 v249, 16, v83
	v_and_b32_e32 v250, 0xffff0000, v83
	v_sub_f32_e32 v249, v84, v249
	v_sub_f32_e32 v250, v85, v250
	v_cvt_pk_bf16_f32 v247, v249, v250
	v_cvt_pk_bf16_f32 v84, v86, v87
	s_nop 0
	v_lshlrev_b32_e32 v249, 16, v84
	v_and_b32_e32 v250, 0xffff0000, v84
	v_sub_f32_e32 v249, v86, v249
	v_sub_f32_e32 v250, v87, v250
	v_cvt_pk_bf16_f32 v248, v249, v250
	v_cvt_pk_bf16_f32 v85, v88, v89
	s_nop 0
	v_lshlrev_b32_e32 v249, 16, v85
	v_and_b32_e32 v250, 0xffff0000, v85
	v_sub_f32_e32 v249, v88, v249
	v_sub_f32_e32 v250, v89, v250
	v_cvt_pk_bf16_f32 v89, v249, v250
	v_mov_b32_e32 v82, v243
	v_mov_b32_e32 v86, v246
	v_mov_b32_e32 v87, v247
	v_mov_b32_e32 v88, v248
	s_waitcnt vmcnt(32)
	v_cvt_pk_bf16_f32 v243, v90, v91
	s_nop 0
	v_lshlrev_b32_e32 v249, 16, v243
	v_and_b32_e32 v250, 0xffff0000, v243
	v_sub_f32_e32 v249, v90, v249
	v_sub_f32_e32 v250, v91, v250
	v_cvt_pk_bf16_f32 v246, v249, v250
	v_cvt_pk_bf16_f32 v91, v92, v93
	s_nop 0
	v_lshlrev_b32_e32 v249, 16, v91
	v_and_b32_e32 v250, 0xffff0000, v91
	v_sub_f32_e32 v249, v92, v249
	v_sub_f32_e32 v250, v93, v250
	v_cvt_pk_bf16_f32 v247, v249, v250
	v_cvt_pk_bf16_f32 v92, v94, v95
	s_nop 0
	v_lshlrev_b32_e32 v249, 16, v92
	v_and_b32_e32 v250, 0xffff0000, v92
	v_sub_f32_e32 v249, v94, v249
	v_sub_f32_e32 v250, v95, v250
	v_cvt_pk_bf16_f32 v248, v249, v250
	v_cvt_pk_bf16_f32 v93, v96, v97
	s_nop 0
	v_lshlrev_b32_e32 v249, 16, v93
	v_and_b32_e32 v250, 0xffff0000, v93
	v_sub_f32_e32 v249, v96, v249
	v_sub_f32_e32 v250, v97, v250
	v_cvt_pk_bf16_f32 v97, v249, v250
	v_mov_b32_e32 v90, v243
	v_mov_b32_e32 v94, v246
	v_mov_b32_e32 v95, v247
	v_mov_b32_e32 v96, v248
	s_waitcnt vmcnt(24)
	v_cvt_pk_bf16_f32 v243, v98, v99
	s_nop 0
	v_lshlrev_b32_e32 v249, 16, v243
	v_and_b32_e32 v250, 0xffff0000, v243
	v_sub_f32_e32 v249, v98, v249
	v_sub_f32_e32 v250, v99, v250
	v_cvt_pk_bf16_f32 v246, v249, v250
	v_cvt_pk_bf16_f32 v99, v100, v101
	s_nop 0
	v_lshlrev_b32_e32 v249, 16, v99
	v_and_b32_e32 v250, 0xffff0000, v99
	v_sub_f32_e32 v249, v100, v249
	v_sub_f32_e32 v250, v101, v250
	v_cvt_pk_bf16_f32 v247, v249, v250
	v_cvt_pk_bf16_f32 v100, v102, v103
	s_nop 0
	v_lshlrev_b32_e32 v249, 16, v100
	v_and_b32_e32 v250, 0xffff0000, v100
	v_sub_f32_e32 v249, v102, v249
	v_sub_f32_e32 v250, v103, v250
	v_cvt_pk_bf16_f32 v248, v249, v250
	v_cvt_pk_bf16_f32 v101, v104, v105
	s_nop 0
	v_lshlrev_b32_e32 v249, 16, v101
	v_and_b32_e32 v250, 0xffff0000, v101
	v_sub_f32_e32 v249, v104, v249
	v_sub_f32_e32 v250, v105, v250
	v_cvt_pk_bf16_f32 v105, v249, v250
	v_mov_b32_e32 v98, v243
	v_mov_b32_e32 v102, v246
	v_mov_b32_e32 v103, v247
	v_mov_b32_e32 v104, v248
	s_waitcnt vmcnt(16)
	v_cvt_pk_bf16_f32 v243, v106, v107
	s_nop 0
	v_lshlrev_b32_e32 v249, 16, v243
	v_and_b32_e32 v250, 0xffff0000, v243
	v_sub_f32_e32 v249, v106, v249
	v_sub_f32_e32 v250, v107, v250
	v_cvt_pk_bf16_f32 v246, v249, v250
	v_cvt_pk_bf16_f32 v107, v108, v109
	s_nop 0
	v_lshlrev_b32_e32 v249, 16, v107
	v_and_b32_e32 v250, 0xffff0000, v107
	v_sub_f32_e32 v249, v108, v249
	v_sub_f32_e32 v250, v109, v250
	v_cvt_pk_bf16_f32 v247, v249, v250
	v_cvt_pk_bf16_f32 v108, v110, v111
	s_nop 0
	v_lshlrev_b32_e32 v249, 16, v108
	v_and_b32_e32 v250, 0xffff0000, v108
	v_sub_f32_e32 v249, v110, v249
	v_sub_f32_e32 v250, v111, v250
	v_cvt_pk_bf16_f32 v248, v249, v250
	v_cvt_pk_bf16_f32 v109, v112, v113
	s_nop 0
	v_lshlrev_b32_e32 v249, 16, v109
	v_and_b32_e32 v250, 0xffff0000, v109
	v_sub_f32_e32 v249, v112, v249
	v_sub_f32_e32 v250, v113, v250
	v_cvt_pk_bf16_f32 v113, v249, v250
	v_mov_b32_e32 v106, v243
	v_mov_b32_e32 v110, v246
	v_mov_b32_e32 v111, v247
	v_mov_b32_e32 v112, v248
	s_waitcnt vmcnt(8)
; __device__ __forceinline__ unsigned cvt_pk_bf16(float lo, float hi) { unsigned r; asm volatile("v_cvt_pk_bf16_f32 %0, %1, %2" : "=v"(r) : "v"(lo), "v"(hi)); return r; }
; #define P5_BAR() asm volatile("s_waitcnt lgkmcnt(0)\n\ts_barrier" ::: "memory")
; __device__ __forceinline__ void phase5(Frame& F, const Args& a) {
;     ...
;             for (int nt = 0; nt < 2; ++nt) { float w8[8];
; #pragma unroll
;                 for (int t = 0; t < 8; ++t) w8[t] = wp[(size_t)(32 * sk + t) * NE + 16 * nt];
;                 pg8::u32x4 hv, lv;
; #pragma unroll
;                 for (int t2 = 0; t2 < 4; ++t2) { const unsigned h = pg8::cvt_pk_bf16(w8[2 * t2], w8[2 * t2 + 1]); hv[t2] = h; lv[t2] = pg8::cvt_pk_bf16(w8[2 * t2] - bflo(h), w8[2 * t2 + 1] - bfhi(h)); }
;                 wh[sk][nt] = __builtin_bit_cast(bf16x8_t, hv); wl[sk][nt] = __builtin_bit_cast(bf16x8_t, lv); } }
;     const float rbv = a.rb[lane & 31];
;     v2u ynx[8];
; #pragma unroll
;     for (int j = 0; j < 8; ++j) ynx[j] = *((const v2u*)(Y1 + (size_t)(row_base + wid) * D) + lane + 64 * j);
;     P5_BAR();
	v_cvt_pk_bf16_f32 v243, v114, v115
	s_nop 0
	v_lshlrev_b32_e32 v249, 16, v243
	v_and_b32_e32 v250, 0xffff0000, v243
	v_sub_f32_e32 v249, v114, v249
	v_sub_f32_e32 v250, v115, v250
	v_cvt_pk_bf16_f32 v246, v249, v250
	v_cvt_pk_bf16_f32 v115, v116, v117
	s_nop 0
	v_lshlrev_b32_e32 v249, 16, v115
	v_and_b32_e32 v250, 0xffff0000, v115
	v_sub_f32_e32 v249, v116, v249
	v_sub_f32_e32 v250, v117, v250
	v_cvt_pk_bf16_f32 v247, v249, v250
	v_cvt_pk_bf16_f32 v116, v118, v119
	s_nop 0
	v_lshlrev_b32_e32 v249, 16, v116
	v_and_b32_e32 v250, 0xffff0000, v116
	v_sub_f32_e32 v249, v118, v249
	v_sub_f32_e32 v250, v119, v250
	v_cvt_pk_bf16_f32 v248, v249, v250
	v_cvt_pk_bf16_f32 v117, v120, v121
	s_nop 0
	v_lshlrev_b32_e32 v249, 16, v117
	v_and_b32_e32 v250, 0xffff0000, v117
	v_sub_f32_e32 v249, v120, v249
	v_sub_f32_e32 v250, v121, v250
	v_cvt_pk_bf16_f32 v121, v249, v250
	v_mov_b32_e32 v114, v243
	v_mov_b32_e32 v118, v246
	v_mov_b32_e32 v119, v247
	v_mov_b32_e32 v120, v248
	s_waitcnt vmcnt(0)
	v_cvt_pk_bf16_f32 v243, v122, v123
	s_nop 0
	v_lshlrev_b32_e32 v249, 16, v243
	v_and_b32_e32 v250, 0xffff0000, v243
	v_sub_f32_e32 v249, v122, v249
	v_sub_f32_e32 v250, v123, v250
	v_cvt_pk_bf16_f32 v246, v249, v250
	v_cvt_pk_bf16_f32 v123, v124, v125
	s_nop 0
	v_lshlrev_b32_e32 v249, 16, v123
	v_and_b32_e32 v250, 0xffff0000, v123
	v_sub_f32_e32 v249, v124, v249
	v_sub_f32_e32 v250, v125, v250
	v_cvt_pk_bf16_f32 v247, v249, v250
	v_cvt_pk_bf16_f32 v124, v126, v127
	s_nop 0
	v_lshlrev_b32_e32 v249, 16, v124
	v_and_b32_e32 v250, 0xffff0000, v124
	v_sub_f32_e32 v249, v126, v249
	v_sub_f32_e32 v250, v127, v250
	v_cvt_pk_bf16_f32 v248, v249, v250
	v_cvt_pk_bf16_f32 v125, v128, v129
	s_nop 0
	v_lshlrev_b32_e32 v249, 16, v125
	v_and_b32_e32 v250, 0xffff0000, v125
	v_sub_f32_e32 v249, v128, v249
	v_sub_f32_e32 v250, v129, v250
	v_cvt_pk_bf16_f32 v129, v249, v250
	v_mov_b32_e32 v122, v243
	v_mov_b32_e32 v126, v246
	v_mov_b32_e32 v127, v247
	v_mov_b32_e32 v128, v248
	global_load_dword v139, v137, s[64:65]
	global_load_dwordx2 v[142:143], v130, s[4:5]
	global_load_dwordx2 v[144:145], v130, s[4:5] offset:512
	global_load_dwordx2 v[146:147], v130, s[4:5] offset:1024
	global_load_dwordx2 v[148:149], v130, s[4:5] offset:1536
	global_load_dwordx2 v[150:151], v130, s[4:5] offset:2048
	global_load_dwordx2 v[152:153], v130, s[4:5] offset:2560
	global_load_dwordx2 v[154:155], v130, s[4:5] offset:3072
	global_load_dwordx2 v[156:157], v130, s[4:5] offset:3584
	s_waitcnt lgkmcnt(0)
	s_barrier
	s_cbranch_scc0 .LBB0_636
	s_add_u32 s20, s76, 0xa00000
	s_addc_u32 s21, s77, 0
	s_add_u32 s22, s76, 0xa40000
	s_addc_u32 s23, s77, 0
	v_lshlrev_b32_e32 v160, 4, v133
	s_add_i32 s4, 0, 0x19800
	v_add_u32_e32 v196, s4, v160
	s_add_i32 s4, 0, 0x1b800
	v_and_b32_e32 v136, 1, v138
	v_and_b32_e32 v134, 0x1f0, v130
	v_mov_b32_e32 v135, v141
	v_add_u32_e32 v197, s4, v160
	v_lshl_add_u64 v[134:135], s[76:77], 0, v[134:135]
	v_cmp_eq_u32_e64 s[4:5], 0, v136
	v_lshlrev_b32_e32 v136, 9, v136
	v_mov_b32_e32 v137, v141
	v_lshl_add_u64 v[134:135], v[134:135], 0, v[136:137]
	s_mov_b64 s[6:7], 0x24000000
	v_lshl_add_u64 v[158:159], v[134:135], 0, s[6:7]
	s_add_i32 s6, 0, 0x1d800
	v_add_u32_e32 v198, s6, v160
	s_add_i32 s6, 0, 0x1f800
	v_add_u32_e32 v199, s6, v160
	s_mul_i32 s6, s49, 0x1010
	v_lshlrev_b32_e32 v164, 2, v133
	s_add_i32 s6, s6, 0
	v_and_b32_e32 v136, 3, v138
	v_and_b32_e32 v134, 0xf0, v164
	v_mov_b32_e32 v135, v141
	s_add_i32 s19, 0, 0x10800
	v_add_u32_e32 v200, s6, v130
	v_lshl_add_u64 v[134:135], s[76:77], 0, v[134:135]
	v_cmp_gt_u32_e64 s[6:7], 2, v136
	v_lshlrev_b32_e32 v136, 8, v136
	s_lshl_b32 s26, s49, 10
	v_lshl_add_u64 v[134:135], v[134:135], 0, v[136:137]
	s_mov_b64 s[8:9], 0x5b000000
	s_lshl_b32 s24, s49, 7
	s_lshl_b32 s25, s49, 2
	s_add_i32 s26, s26, s19
	v_lshl_add_u64 v[160:161], v[134:135], 0, s[8:9]
	v_and_b32_e32 v134, 7, v138
	s_movk_i32 s10, 0x808
	s_add_u32 s35, s76, 0xe20000
	v_lshl_add_u32 v165, v1, 2, s19
	v_mad_u32_u24 v134, v134, s10, v140
	s_addc_u32 s36, s77, 0
	s_lshl_b32 s19, s49, 4
	v_lshl_add_u32 v201, v134, 1, 0
	v_lshlrev_b32_e32 v134, 9, v131
	v_mov_b32_e32 v131, v141
	s_add_i32 s19, s19, 0
	s_lshl_b32 s18, s18, 2
	v_lshl_add_u64 v[162:163], s[12:13], 0, v[130:131]
	v_lshl_add_u32 v130, v132, 2, s26
	v_add_u32_e32 v131, s19, v164
	s_add_i32 s18, s18, s25
	s_mov_b32 s34, 0
	v_cmp_eq_u32_e64 s[8:9], 0, v133
	v_cmp_gt_u32_e64 s[10:11], 32, v133
	v_cmp_gt_u32_e64 s[12:13], 4, v133
	v_cmp_eq_u32_e64 s[14:15], 1, v133
	v_cmp_eq_u32_e64 s[16:17], 2, v133
	v_add_u32_e32 v202, 0x18400, v131
	v_add_u32_e32 v164, s18, v133
	v_mov_b32_e32 v203, 0x3727c5ac
	s_mov_b32 s37, 0xf800000
	v_mov_b32_e32 v204, 0x260
	s_movk_i32 s38, 0x7fff
	s_mov_b32 s39, 0x1e3ce508
	s_mov_b32 s40, 0x42fe0000
	s_mov_b32 s41, 0x4b3fff81
	s_mov_b32 s42, 0xc0c0400
	s_mov_b32 s43, 0x4000c0c
	v_add_u32_e32 v205, v130, v134
	v_add_u32_e32 v206, s24, v165
	v_mov_b32_e32 v207, 1
	v_mov_b32_e32 v208, 0x4b40007f
	v_mov_b32_e32 v209, 0xff61b1e6
	s_branch .LBB0_627
